# speedup vs baseline: 1.0134x; 1.0134x over previous
_Z13select_kernelPKfPyPiS2_:
	s_load_dwordx8 s[4:11], s[0:1], 0x0
	v_lshrrev_b32_e32 v1, 6, v0
	v_and_b32_e32 v4, 63, v0
	v_lshl_or_b32 v2, s2, 2, v1
	v_lshlrev_b32_e32 v0, 2, v4
	v_mov_b32_e32 v1, 0
	s_movk_i32 s0, 0x320
	v_mad_i64_i32 v[0:1], s[0:1], v2, s0, v[0:1]
	v_ashrrev_i32_e32 v3, 31, v2
	v_or_b32_e32 v6, 0xffffffc0, v4
	s_waitcnt lgkmcnt(0)
	v_lshl_add_u64 v[0:1], s[4:5], 0, v[0:1]
	global_load_dword v11, v[0:1], off
	global_load_dword v12, v[0:1], off offset:256
	global_load_dword v13, v[0:1], off offset:512
	v_cmp_gt_u32_e32 vcc, 8, v4
	s_and_saveexec_b64 s[12:13], vcc
	global_load_dword v14, v[0:1], off offset:768
	s_or_b64 exec, exec, s[12:13]
	v_mov_b32_e32 v5, 0x7f800000
	v_mov_b32_e32 v7, 0xff800000
	v_mov_b32_e32 v9, 0xff800000
	s_waitcnt vmcnt(3)
	v_cmp_gt_f32_e32 vcc, v11, v7
	v_max_f32_e32 v9, v9, v11
	v_min_f32_e32 v5, v5, v11
	v_cndmask_b32_e32 v9, v9, v7, vcc
	v_max_f32_e32 v7, v7, v11
	s_waitcnt vmcnt(2)
	v_cmp_gt_f32_e32 vcc, v12, v7
	v_max_f32_e32 v9, v9, v12
	v_min_f32_e32 v5, v5, v12
	v_cndmask_b32_e32 v9, v9, v7, vcc
	v_max_f32_e32 v7, v7, v12
	s_waitcnt vmcnt(1)
	v_cmp_gt_f32_e32 vcc, v13, v7
	v_max_f32_e32 v9, v9, v13
	v_min_f32_e32 v5, v5, v13
	v_cndmask_b32_e32 v9, v9, v7, vcc
	v_max_f32_e32 v7, v7, v13
	s_waitcnt vmcnt(0)
	v_cmp_gt_u32_e32 vcc, 8, v4
	s_and_saveexec_b64 s[12:13], vcc
	v_cmp_gt_f32_e32 vcc, v14, v7
	v_max_f32_e32 v9, v9, v14
	v_min_f32_e32 v5, v5, v14
	v_cndmask_b32_e32 v9, v9, v7, vcc
	v_max_f32_e32 v7, v7, v14
	s_or_b64 exec, exec, s[12:13]
	v_mbcnt_lo_u32_b32 v0, -1, 0
	v_mbcnt_hi_u32_b32 v0, -1, v0
	v_and_b32_e32 v1, 64, v0
	v_add_u32_e32 v1, 64, v1
	v_xor_b32_e32 v6, 32, v0
	v_cmp_lt_i32_e32 vcc, v6, v1
	v_max_f32_e32 v11, v7, v7
	s_nop 0
	v_cndmask_b32_e32 v6, v0, v6, vcc
	v_lshlrev_b32_e32 v6, 2, v6
	ds_bpermute_b32 v8, v6, v9
	ds_bpermute_b32 v10, v6, v7
	v_max_f32_e32 v9, v9, v9
	ds_bpermute_b32 v6, v6, v5
	v_max_f32_e32 v5, v5, v5
	s_waitcnt lgkmcnt(2)
	v_max_f32_e32 v8, v8, v8
	v_max_f32_e32 v8, v11, v8
	s_waitcnt lgkmcnt(1)
	v_max_f32_e32 v11, v10, v10
	v_max_f32_e32 v9, v9, v11
	v_cmp_lt_f32_e32 vcc, v7, v10
	s_waitcnt lgkmcnt(0)
	v_max_f32_e32 v6, v6, v6
	v_min_f32_e32 v5, v5, v6
	v_cndmask_b32_e32 v8, v9, v8, vcc
	v_xor_b32_e32 v9, 16, v0
	v_cndmask_b32_e32 v7, v7, v10, vcc
	v_cmp_lt_i32_e32 vcc, v9, v1
	s_nop 1
	v_cndmask_b32_e32 v9, v0, v9, vcc
	v_lshlrev_b32_e32 v9, 2, v9
	ds_bpermute_b32 v10, v9, v8
	ds_bpermute_b32 v11, v9, v7
	s_waitcnt lgkmcnt(1)
	v_max_f32_e32 v6, v10, v10
	v_max_f32_e32 v10, v7, v7
	v_max_f32_e32 v6, v10, v6
	s_waitcnt lgkmcnt(0)
	v_max_f32_e32 v10, v11, v11
	v_max_f32_e32 v8, v8, v10
	v_cmp_lt_f32_e32 vcc, v7, v11
	s_nop 1
	v_cndmask_b32_e32 v6, v8, v6, vcc
	ds_bpermute_b32 v8, v9, v5
	v_xor_b32_e32 v9, 8, v0
	v_cmp_lt_i32_e64 s[0:1], v9, v1
	v_cndmask_b32_e32 v7, v7, v11, vcc
	s_waitcnt lgkmcnt(0)
	v_max_f32_e32 v8, v8, v8
	v_cndmask_b32_e64 v9, v0, v9, s[0:1]
	v_lshlrev_b32_e32 v9, 2, v9
	ds_bpermute_b32 v10, v9, v6
	ds_bpermute_b32 v11, v9, v7
	v_min_f32_e32 v5, v5, v8
	s_waitcnt lgkmcnt(1)
	v_max_f32_e32 v8, v10, v10
	v_max_f32_e32 v10, v7, v7
	v_max_f32_e32 v8, v10, v8
	s_waitcnt lgkmcnt(0)
	v_max_f32_e32 v10, v11, v11
	v_max_f32_e32 v6, v6, v10
	v_cmp_lt_f32_e32 vcc, v7, v11
	s_nop 1
	v_cndmask_b32_e32 v6, v6, v8, vcc
	ds_bpermute_b32 v8, v9, v5
	v_xor_b32_e32 v9, 4, v0
	v_cmp_lt_i32_e64 s[0:1], v9, v1
	v_cndmask_b32_e32 v7, v7, v11, vcc
	s_waitcnt lgkmcnt(0)
	v_max_f32_e32 v8, v8, v8
	v_cndmask_b32_e64 v9, v0, v9, s[0:1]
	v_lshlrev_b32_e32 v9, 2, v9
	ds_bpermute_b32 v10, v9, v6
	ds_bpermute_b32 v11, v9, v7
	v_min_f32_e32 v5, v5, v8
	s_waitcnt lgkmcnt(1)
	v_max_f32_e32 v8, v10, v10
	v_max_f32_e32 v10, v7, v7
	v_max_f32_e32 v8, v10, v8
	s_waitcnt lgkmcnt(0)
	v_max_f32_e32 v10, v11, v11
	v_max_f32_e32 v6, v6, v10
	v_cmp_lt_f32_e32 vcc, v7, v11
	s_nop 1
	v_cndmask_b32_e32 v6, v6, v8, vcc
	ds_bpermute_b32 v8, v9, v5
	v_xor_b32_e32 v9, 2, v0
	v_cmp_lt_i32_e64 s[0:1], v9, v1
	v_cndmask_b32_e32 v7, v7, v11, vcc
	s_waitcnt lgkmcnt(0)
	v_max_f32_e32 v8, v8, v8
	v_cndmask_b32_e64 v9, v0, v9, s[0:1]
	v_lshlrev_b32_e32 v9, 2, v9
	ds_bpermute_b32 v10, v9, v6
	ds_bpermute_b32 v11, v9, v7
	v_min_f32_e32 v5, v5, v8
	s_waitcnt lgkmcnt(1)
	v_max_f32_e32 v8, v10, v10
	v_max_f32_e32 v10, v7, v7
	v_max_f32_e32 v8, v10, v8
	s_waitcnt lgkmcnt(0)
	v_max_f32_e32 v10, v11, v11
	v_max_f32_e32 v6, v6, v10
	v_cmp_lt_f32_e32 vcc, v7, v11
	s_nop 1
	v_cndmask_b32_e32 v6, v6, v8, vcc
	ds_bpermute_b32 v8, v9, v5
	v_xor_b32_e32 v9, 1, v0
	v_cmp_lt_i32_e64 s[0:1], v9, v1
	v_cndmask_b32_e32 v7, v7, v11, vcc
	s_waitcnt lgkmcnt(0)
	v_max_f32_e32 v8, v8, v8
	v_cndmask_b32_e64 v0, v0, v9, s[0:1]
	v_lshlrev_b32_e32 v0, 2, v0
	ds_bpermute_b32 v1, v0, v6
	ds_bpermute_b32 v9, v0, v7
	v_min_f32_e32 v5, v5, v8
	ds_bpermute_b32 v0, v0, v5
	v_max_f32_e32 v8, v7, v7
	s_waitcnt lgkmcnt(2)
	v_max_f32_e32 v1, v1, v1
	v_max_f32_e32 v1, v8, v1
	s_waitcnt lgkmcnt(1)
	v_max_f32_e32 v8, v9, v9
	v_max_f32_e32 v6, v6, v8
	v_cmp_lt_f32_e32 vcc, v7, v9
	s_waitcnt lgkmcnt(0)
	v_max_f32_e32 v0, v0, v0
	v_min_f32_e32 v0, v5, v0
	v_cndmask_b32_e32 v1, v6, v1, vcc
	v_cndmask_b32_e32 v6, v7, v9, vcc
	v_sub_f32_e32 v0, v6, v0
	v_mul_f32_e32 v0, 0x3a83126f, v0
	v_max_f32_e32 v0, 0x3b449ba6, v0
	v_sub_f32_e32 v1, v6, v1
	v_cmp_eq_u32_e32 vcc, 0, v4
	v_cmp_nge_f32_e64 s[0:1], v1, v0
	s_and_b64 s[0:1], vcc, s[0:1]
	s_and_saveexec_b64 s[2:3], s[0:1]
	s_cbranch_execz .LBB1_10
	s_mov_b64 s[2:3], exec
	v_mbcnt_lo_u32_b32 v0, s2, 0
	v_mbcnt_hi_u32_b32 v0, s3, v0
	v_cmp_eq_u32_e32 vcc, 0, v0
	s_and_saveexec_b64 s[0:1], vcc
	s_cbranch_execz .LBB1_9
	s_bcnt1_i32_b64 s2, s[2:3]
	v_mov_b32_e32 v1, 0
	v_mov_b32_e32 v4, s2
	global_atomic_add v1, v1, v4, s[10:11] sc0

	.amdhsa_kernel _Z13select_kernelPKfPyPiS2_
		.amdhsa_group_segment_fixed_size 0
		.amdhsa_private_segment_fixed_size 0
		.amdhsa_kernarg_size 32
		.amdhsa_user_sgpr_count 2
		.amdhsa_user_sgpr_dispatch_ptr 0
		.amdhsa_user_sgpr_queue_ptr 0
		.amdhsa_user_sgpr_kernarg_segment_ptr 1
		.amdhsa_user_sgpr_dispatch_id 0
		.amdhsa_user_sgpr_kernarg_preload_length 0
		.amdhsa_user_sgpr_kernarg_preload_offset 0
		.amdhsa_user_sgpr_private_segment_size 0
		.amdhsa_uses_dynamic_stack 0
		.amdhsa_enable_private_segment 0
		.amdhsa_system_sgpr_workgroup_id_x 1
		.amdhsa_system_sgpr_workgroup_id_y 0
		.amdhsa_system_sgpr_workgroup_id_z 0
		.amdhsa_system_sgpr_workgroup_info 0
		.amdhsa_system_vgpr_workitem_id 0
		.amdhsa_next_free_vgpr 16
		.amdhsa_next_free_sgpr 15
		.amdhsa_accum_offset 16
		.amdhsa_reserve_vcc 1
		.amdhsa_float_round_mode_32 0
		.amdhsa_float_round_mode_16_64 0
		.amdhsa_float_denorm_mode_32 3
		.amdhsa_float_denorm_mode_16_64 3
		.amdhsa_dx10_clamp 1
		.amdhsa_ieee_mode 1
		.amdhsa_fp16_overflow 0
		.amdhsa_tg_split 0
		.amdhsa_exception_fp_ieee_invalid_op 0
		.amdhsa_exception_fp_denorm_src 0
		.amdhsa_exception_fp_ieee_div_zero 0
		.amdhsa_exception_fp_ieee_overflow 0
		.amdhsa_exception_fp_ieee_underflow 0
		.amdhsa_exception_fp_ieee_inexact 0
		.amdhsa_exception_int_div_zero 0
	.end_amdhsa_kernel

.LBB2_4:
	s_or_b64 exec, exec, s[8:9]
	v_lshlrev_b32_e32 v1, 3, v0
	s_waitcnt lgkmcnt(0)
	global_load_dword v13, v1, s[6:7]
	v_or_b32_e32 v1, 0x400, v0
	v_lshlrev_b32_e32 v3, 3, v1
	global_load_dword v14, v3, s[6:7]
	v_or_b32_e32 v2, 0x800, v0
	v_lshlrev_b32_e32 v6, 3, v2
	global_load_dword v15, v6, s[6:7]
	v_or_b32_e32 v3, 0xc00, v0
	v_lshlrev_b32_e32 v10, 3, v3
	global_load_dword v16, v10, s[6:7]
	s_barrier
	v_mov_b32_e32 v4, 1
	v_mov_b32_e32 v12, 0
	v_mov_b32_e32 v11, 0
	v_lshrrev_b32_e32 v10, 6, v0
	s_waitcnt vmcnt(3)
	v_min_i32_e32 v13, -1, v13
	v_max_u32_e32 v13, 0xffffff38, v13
	v_not_b32_e32 v13, v13
	v_lshlrev_b32_e32 v5, 2, v13
	ds_add_u32 v5, v4
	s_waitcnt vmcnt(2)
	v_min_i32_e32 v14, -1, v14
	v_max_u32_e32 v14, 0xffffff38, v14
	v_not_b32_e32 v14, v14
	v_lshlrev_b32_e32 v7, 2, v14
	ds_add_u32 v7, v4
	s_waitcnt vmcnt(1)
	v_min_i32_e32 v15, -1, v15
	v_max_u32_e32 v15, 0xffffff38, v15
	v_not_b32_e32 v15, v15
	v_lshlrev_b32_e32 v8, 2, v15
	ds_add_u32 v8, v4
	s_waitcnt vmcnt(0)
	v_min_i32_e32 v16, -1, v16
	v_max_u32_e32 v16, 0xffffff38, v16
	v_not_b32_e32 v16, v16
	v_lshlrev_b32_e32 v6, 2, v16
	ds_add_u32 v6, v4
	v_mov_b32_e32 v4, 0
	s_waitcnt lgkmcnt(0)
	s_barrier
	s_and_saveexec_b64 s[6:7], vcc
	s_cbranch_execz .LBB2_8
	v_lshlrev_b32_e32 v4, 2, v0
	ds_read_b32 v4, v4
	v_mbcnt_lo_u32_b32 v9, -1, 0
	v_mbcnt_hi_u32_b32 v9, -1, v9
	v_and_b32_e32 v12, 64, v9
	v_add_u32_e32 v13, -1, v9
	v_cmp_lt_i32_e64 s[2:3], v13, v12
	s_waitcnt lgkmcnt(0)
	v_add_u32_e32 v11, 31, v4
	v_ashrrev_i32_e32 v11, 5, v11
	v_cndmask_b32_e64 v13, v13, v9, s[2:3]
	v_lshlrev_b32_e32 v13, 2, v13
	ds_bpermute_b32 v14, v13, v11
	ds_bpermute_b32 v13, v13, v4
	v_and_b32_e32 v15, 63, v0
	v_cmp_eq_u32_e64 s[2:3], 0, v15
	v_add_u32_e32 v16, -2, v9
	s_waitcnt lgkmcnt(1)
	v_cndmask_b32_e64 v14, v14, 0, s[2:3]
	s_waitcnt lgkmcnt(0)
	v_cndmask_b32_e64 v13, v13, 0, s[2:3]
	v_cmp_lt_i32_e64 s[2:3], v16, v12
	v_add_u32_e32 v14, v14, v11
	v_add_u32_e32 v13, v13, v4
	v_cndmask_b32_e64 v16, v16, v9, s[2:3]
	v_lshlrev_b32_e32 v16, 2, v16
	ds_bpermute_b32 v17, v16, v14
	ds_bpermute_b32 v16, v16, v13
	v_cmp_gt_u32_e64 s[2:3], 2, v15
	s_waitcnt lgkmcnt(1)
	s_nop 0
	v_cndmask_b32_e64 v17, v17, 0, s[2:3]
	v_add_u32_e32 v14, v17, v14
	v_add_u32_e32 v17, -4, v9
	s_waitcnt lgkmcnt(0)
	v_cndmask_b32_e64 v16, v16, 0, s[2:3]
	v_cmp_lt_i32_e64 s[2:3], v17, v12
	v_add_u32_e32 v13, v16, v13
	s_nop 0
	v_cndmask_b32_e64 v17, v17, v9, s[2:3]
	v_lshlrev_b32_e32 v17, 2, v17
	ds_bpermute_b32 v18, v17, v14
	ds_bpermute_b32 v16, v17, v13
	v_cmp_gt_u32_e64 s[2:3], 4, v15
	s_waitcnt lgkmcnt(1)
	s_nop 0
	v_cndmask_b32_e64 v17, v18, 0, s[2:3]
	v_add_u32_e32 v14, v17, v14
	v_add_u32_e32 v17, -8, v9
	s_waitcnt lgkmcnt(0)
	v_cndmask_b32_e64 v16, v16, 0, s[2:3]
	v_cmp_lt_i32_e64 s[2:3], v17, v12
	v_add_u32_e32 v13, v16, v13
	s_nop 0
	v_cndmask_b32_e64 v17, v17, v9, s[2:3]
	v_lshlrev_b32_e32 v17, 2, v17
	ds_bpermute_b32 v18, v17, v14
	ds_bpermute_b32 v16, v17, v13
	v_cmp_gt_u32_e64 s[2:3], 8, v15
	s_waitcnt lgkmcnt(1)
	s_nop 0
	v_cndmask_b32_e64 v17, v18, 0, s[2:3]
	v_add_u32_e32 v14, v17, v14
	v_add_u32_e32 v17, -16, v9
	s_waitcnt lgkmcnt(0)
	v_cndmask_b32_e64 v16, v16, 0, s[2:3]
	v_cmp_lt_i32_e64 s[2:3], v17, v12
	v_add_u32_e32 v13, v16, v13
	s_nop 0
	v_cndmask_b32_e64 v17, v17, v9, s[2:3]
	v_lshlrev_b32_e32 v17, 2, v17
	ds_bpermute_b32 v18, v17, v14
	ds_bpermute_b32 v16, v17, v13
	v_cmp_gt_u32_e64 s[2:3], 16, v15
	s_waitcnt lgkmcnt(1)
	s_nop 0
	v_cndmask_b32_e64 v17, v18, 0, s[2:3]
	v_add_u32_e32 v14, v17, v14
	v_subrev_u32_e32 v17, 32, v9
	s_waitcnt lgkmcnt(0)
	v_cndmask_b32_e64 v16, v16, 0, s[2:3]
	v_cmp_lt_i32_e64 s[2:3], v17, v12
	v_add_u32_e32 v13, v16, v13
	s_nop 0
	v_cndmask_b32_e64 v9, v17, v9, s[2:3]
	v_lshlrev_b32_e32 v9, 2, v9
	ds_bpermute_b32 v12, v9, v14
	ds_bpermute_b32 v16, v9, v13
	v_cmp_gt_u32_e64 s[2:3], 32, v15
	s_waitcnt lgkmcnt(1)
	s_nop 0
	v_cndmask_b32_e64 v9, v12, 0, s[2:3]
	s_waitcnt lgkmcnt(0)
	v_cndmask_b32_e64 v12, v16, 0, s[2:3]
	v_add_u32_e32 v9, v9, v14
	v_add_u32_e32 v12, v12, v13
	v_cmp_eq_u32_e64 s[2:3], 63, v15
	s_and_saveexec_b64 s[8:9], s[2:3]
	v_lshlrev_b32_e32 v13, 2, v10
	v_add_u32_e32 v13, 0x1000, v13
	ds_write2_b32 v13, v12, v9 offset1:4
	s_or_b64 exec, exec, s[8:9]

.LBB10_6:
	v_ashrrev_i32_e32 v47, 31, v46
	v_lshl_add_u64 v[54:55], v[46:47], 2, s[24:25]
	global_load_dword v44, v[54:55], off
	global_load_dword v1, v[2:3], off
	s_or_b64 exec, exec, s[22:23]
	s_waitcnt lgkmcnt(0)
	s_cmp_ge_i32 s19, s2
	s_mov_b64 s[22:23], -1
	s_cbranch_scc1 .LBB10_3

amdhsa.kernels:
  - .agpr_count:     0
    .args:
      - .actual_access:  read_only
        .address_space:  global
        .offset:         0
        .size:           8
        .value_kind:     global_buffer
      - .actual_access:  write_only
        .address_space:  global
        .offset:         8
        .size:           8
        .value_kind:     global_buffer
      - .actual_access:  read_only
        .address_space:  global
        .offset:         16
        .size:           8
        .value_kind:     global_buffer
      - .actual_access:  read_only
        .address_space:  global
        .offset:         24
        .size:           8
        .value_kind:     global_buffer
      - .actual_access:  read_only
        .address_space:  global
        .offset:         32
        .size:           8
        .value_kind:     global_buffer
      - .actual_access:  write_only
        .address_space:  global
        .offset:         40
        .size:           8
        .value_kind:     global_buffer
      - .actual_access:  write_only
        .address_space:  global
        .offset:         48
        .size:           8
        .value_kind:     global_buffer
      - .actual_access:  write_only
        .address_space:  global
        .offset:         56
        .size:           8
        .value_kind:     global_buffer
      - .actual_access:  write_only
        .address_space:  global
        .offset:         64
        .size:           8
        .value_kind:     global_buffer
      - .actual_access:  write_only
        .address_space:  global
        .offset:         72
        .size:           8
        .value_kind:     global_buffer
      - .actual_access:  write_only
        .address_space:  global
        .offset:         80
        .size:           8
        .value_kind:     global_buffer
    .group_segment_fixed_size: 16640
    .kernarg_segment_align: 8
    .kernarg_segment_size: 88
    .language:       OpenCL C
    .language_version:
      - 2
      - 0
    .max_flat_workgroup_size: 256
    .name:           _Z8prep_allPKfPcS0_S0_S0_S1_S1_S1_PyPiS3_
    .private_segment_fixed_size: 0
    .sgpr_count:     30
    .sgpr_spill_count: 0
    .symbol:         _Z8prep_allPKfPcS0_S0_S0_S1_S1_S1_PyPiS3_.kd
    .uniform_work_group_size: 1
    .uses_dynamic_stack: false
    .vgpr_count:     48
    .vgpr_spill_count: 0
    .wavefront_size: 64
  - .agpr_count:     0
    .args:
      - .actual_access:  read_only
        .address_space:  global
        .offset:         0
        .size:           8
        .value_kind:     global_buffer
      - .actual_access:  write_only
        .address_space:  global
        .offset:         8
        .size:           8
        .value_kind:     global_buffer
      - .actual_access:  write_only
        .address_space:  global
        .offset:         16
        .size:           8
        .value_kind:     global_buffer
      - .address_space:  global
        .offset:         24
        .size:           8
        .value_kind:     global_buffer
    .group_segment_fixed_size: 0
    .kernarg_segment_align: 8
    .kernarg_segment_size: 32
    .language:       OpenCL C
    .language_version:
      - 2
      - 0
    .max_flat_workgroup_size: 256
    .name:           _Z13select_kernelPKfPyPiS2_
    .private_segment_fixed_size: 0
    .sgpr_count:     21
    .sgpr_spill_count: 0
    .symbol:         _Z13select_kernelPKfPyPiS2_.kd
    .uniform_work_group_size: 1
    .uses_dynamic_stack: false
    .vgpr_count:     16
    .vgpr_spill_count: 0
    .wavefront_size: 64
  - .agpr_count:     0
    .args:
      - .actual_access:  read_only
        .address_space:  global
        .offset:         0
        .size:           8
        .value_kind:     global_buffer
      - .actual_access:  write_only
        .address_space:  global
        .offset:         8
        .size:           8
        .value_kind:     global_buffer
      - .actual_access:  write_only
        .address_space:  global
        .offset:         16
        .size:           8
        .value_kind:     global_buffer
      - .actual_access:  write_only
        .address_space:  global
        .offset:         24
        .size:           8
        .value_kind:     global_buffer
    .group_segment_fixed_size: 4128
    .kernarg_segment_align: 8
    .kernarg_segment_size: 32
    .language:       OpenCL C
    .language_version:
      - 2
      - 0
    .max_flat_workgroup_size: 1024
    .name:           _Z12route_kernelPKyPiP15HIP_vector_typeIiLj4EES1_
    .private_segment_fixed_size: 0
    .sgpr_count:     19
    .sgpr_spill_count: 0
    .symbol:         _Z12route_kernelPKyPiP15HIP_vector_typeIiLj4EES1_.kd
    .uniform_work_group_size: 1
    .uses_dynamic_stack: false
    .vgpr_count:     23
    .vgpr_spill_count: 0
    .wavefront_size: 64
  - .agpr_count:     66
    .args:
      - .actual_access:  read_only
        .address_space:  global
        .offset:         0
        .size:           8
        .value_kind:     global_buffer
      - .actual_access:  read_only
        .address_space:  global
        .offset:         8
        .size:           8
        .value_kind:     global_buffer
      - .actual_access:  read_only
        .address_space:  global
        .offset:         16
        .size:           8
        .value_kind:     global_buffer
      - .actual_access:  read_only
        .address_space:  global
        .offset:         24
        .size:           8
        .value_kind:     global_buffer
      - .actual_access:  read_only
        .address_space:  global
        .offset:         32
        .size:           8
        .value_kind:     global_buffer
      - .actual_access:  write_only
        .address_space:  global
        .offset:         40
        .size:           8
        .value_kind:     global_buffer
    .group_segment_fixed_size: 51200
    .kernarg_segment_align: 8
    .kernarg_segment_size: 48
    .language:       OpenCL C
    .language_version:
      - 2
      - 0
    .max_flat_workgroup_size: 256
    .name:           _Z13expert_kernelPKcPKfPKiPK15HIP_vector_typeIiLj4EES4_Pf
    .private_segment_fixed_size: 0
    .sgpr_count:     20
    .sgpr_spill_count: 0
    .symbol:         _Z13expert_kernelPKcPKfPKiPK15HIP_vector_typeIiLj4EES4_Pf.kd
    .uniform_work_group_size: 1
    .uses_dynamic_stack: false
    .vgpr_count:     154
    .vgpr_spill_count: 0
    .wavefront_size: 64
  - .agpr_count:     0
    .args:
      - .actual_access:  read_only
        .address_space:  global
        .offset:         0
        .size:           8
        .value_kind:     global_buffer
      - .actual_access:  read_only
        .address_space:  global
        .offset:         8
        .size:           8
        .value_kind:     global_buffer
      - .actual_access:  read_only
        .address_space:  global
        .offset:         16
        .size:           8
        .value_kind:     global_buffer
      - .actual_access:  read_only
        .address_space:  global
        .offset:         24
        .size:           8
        .value_kind:     global_buffer
      - .actual_access:  read_only
        .address_space:  global
        .offset:         32
        .size:           8
        .value_kind:     global_buffer
      - .actual_access:  read_only
        .address_space:  global
        .offset:         40
        .size:           8
        .value_kind:     global_buffer
      - .actual_access:  read_only
        .address_space:  global
        .offset:         48
        .size:           8
        .value_kind:     global_buffer
      - .actual_access:  read_only
        .address_space:  global
        .offset:         56
        .size:           8
        .value_kind:     global_buffer
      - .actual_access:  read_only
        .address_space:  global
        .offset:         64
        .size:           8
        .value_kind:     global_buffer
      - .actual_access:  write_only
        .address_space:  global
        .offset:         72
        .size:           8
        .value_kind:     global_buffer
    .group_segment_fixed_size: 14000
    .kernarg_segment_align: 8
    .kernarg_segment_size: 80
    .language:       OpenCL C
    .language_version:
      - 2
      - 0
    .max_flat_workgroup_size: 256
    .name:           _Z12final_kernelPKfPKiPK15HIP_vector_typeIiLj4EES2_S2_S0_S0_S0_S0_Pf
    .private_segment_fixed_size: 0
    .sgpr_count:     50
    .sgpr_spill_count: 0
    .symbol:         _Z12final_kernelPKfPKiPK15HIP_vector_typeIiLj4EES2_S2_S0_S0_S0_S0_Pf.kd
    .uniform_work_group_size: 1
    .uses_dynamic_stack: false
    .vgpr_count:     140
    .vgpr_spill_count: 0
    .wavefront_size: 64
  - .agpr_count:     0
    .args:
      - .address_space:  global
        .offset:         0
        .size:           8
        .value_kind:     global_buffer
      - .address_space:  global
        .offset:         8
        .size:           8
        .value_kind:     global_buffer
      - .offset:         16
        .size:           4
        .value_kind:     by_value
      - .offset:         20
        .size:           4
        .value_kind:     by_value
      - .actual_access:  read_only
        .address_space:  global
        .offset:         24
        .size:           8
        .value_kind:     global_buffer
      - .offset:         32
        .size:           4
        .value_kind:     by_value
      - .actual_access:  read_only
        .address_space:  global
        .offset:         40
        .size:           8
        .value_kind:     global_buffer
      - .actual_access:  read_only
        .address_space:  global
        .offset:         48
        .size:           8
        .value_kind:     global_buffer
      - .actual_access:  write_only
        .address_space:  global
        .offset:         56
        .size:           8
        .value_kind:     global_buffer
      - .offset:         64
        .size:           4
        .value_kind:     by_value
      - .actual_access:  read_only
        .address_space:  global
        .offset:         72
        .size:           8
        .value_kind:     global_buffer
    .group_segment_fixed_size: 0
    .kernarg_segment_align: 8
    .kernarg_segment_size: 80
    .language:       OpenCL C
    .language_version:
      - 2
      - 0
    .max_flat_workgroup_size: 512
    .name:           _Z7gemm_x3ILi2ELi2ELi2ELi0EEvPKcS1_iiPKfiS3_PKiPciPy
    .private_segment_fixed_size: 0
    .sgpr_count:     38
    .sgpr_spill_count: 0
    .symbol:         _Z7gemm_x3ILi2ELi2ELi2ELi0EEvPKcS1_iiPKfiS3_PKiPciPy.kd
    .uniform_work_group_size: 1
    .uses_dynamic_stack: false
    .vgpr_count:     208
    .vgpr_spill_count: 0
    .wavefront_size: 64
  - .agpr_count:     0
    .args:
      - .address_space:  global
        .offset:         0
        .size:           8
        .value_kind:     global_buffer
      - .address_space:  global
        .offset:         8
        .size:           8
        .value_kind:     global_buffer
      - .offset:         16
        .size:           4
        .value_kind:     by_value
      - .offset:         20
        .size:           4
        .value_kind:     by_value
      - .actual_access:  read_only
        .address_space:  global
        .offset:         24
        .size:           8
        .value_kind:     global_buffer
      - .offset:         32
        .size:           4
        .value_kind:     by_value
      - .actual_access:  read_only
        .address_space:  global
        .offset:         40
        .size:           8
        .value_kind:     global_buffer
      - .actual_access:  read_only
        .address_space:  global
        .offset:         48
        .size:           8
        .value_kind:     global_buffer
      - .actual_access:  write_only
        .address_space:  global
        .offset:         56
        .size:           8
        .value_kind:     global_buffer
      - .offset:         64
        .size:           4
        .value_kind:     by_value
      - .actual_access:  read_only
        .address_space:  global
        .offset:         72
        .size:           8
        .value_kind:     global_buffer
    .group_segment_fixed_size: 0
    .kernarg_segment_align: 8
    .kernarg_segment_size: 80
    .language:       OpenCL C
    .language_version:
      - 2
      - 0
    .max_flat_workgroup_size: 512
    .name:           _Z7gemm_x3ILi2ELi2ELi1ELi1EEvPKcS1_iiPKfiS3_PKiPciPy
    .private_segment_fixed_size: 0
    .sgpr_count:     32
    .sgpr_spill_count: 0
    .symbol:         _Z7gemm_x3ILi2ELi2ELi1ELi1EEvPKcS1_iiPKfiS3_PKiPciPy.kd
    .uniform_work_group_size: 1
    .uses_dynamic_stack: false
    .vgpr_count:     114
    .vgpr_spill_count: 0
    .wavefront_size: 64
  - .agpr_count:     32
    .args:
      - .address_space:  global
        .offset:         0
        .size:           8
        .value_kind:     global_buffer
      - .address_space:  global
        .offset:         8
        .size:           8
        .value_kind:     global_buffer
      - .offset:         16
        .size:           4
        .value_kind:     by_value
      - .offset:         20
        .size:           4
        .value_kind:     by_value
      - .actual_access:  read_only
        .address_space:  global
        .offset:         24
        .size:           8
        .value_kind:     global_buffer
      - .offset:         32
        .size:           4
        .value_kind:     by_value
      - .actual_access:  read_only
        .address_space:  global
        .offset:         40
        .size:           8
        .value_kind:     global_buffer
      - .actual_access:  read_only
        .address_space:  global
        .offset:         48
        .size:           8
        .value_kind:     global_buffer
      - .actual_access:  write_only
        .address_space:  global
        .offset:         56
        .size:           8
        .value_kind:     global_buffer
      - .offset:         64
        .size:           4
        .value_kind:     by_value
      - .address_space:  global
        .offset:         72
        .size:           8
        .value_kind:     global_buffer
    .group_segment_fixed_size: 0
    .kernarg_segment_align: 8
    .kernarg_segment_size: 80
    .language:       OpenCL C
    .language_version:
      - 2
      - 0
    .max_flat_workgroup_size: 256
    .name:           _Z7gemm_x3ILi1ELi2ELi1ELi2EEvPKcS1_iiPKfiS3_PKiPciPy
    .private_segment_fixed_size: 0
    .sgpr_count:     29
    .sgpr_spill_count: 0
    .symbol:         _Z7gemm_x3ILi1ELi2ELi1ELi2EEvPKcS1_iiPKfiS3_PKiPciPy.kd
    .uniform_work_group_size: 1
    .uses_dynamic_stack: false
    .vgpr_count:     136
    .vgpr_spill_count: 0
    .wavefront_size: 64
  - .agpr_count:     0
    .args:
      - .actual_access:  read_only
        .address_space:  global
        .offset:         0
        .size:           8
        .value_kind:     global_buffer
      - .offset:         8
        .size:           4
        .value_kind:     by_value
      - .offset:         12
        .size:           4
        .value_kind:     by_value
      - .actual_access:  read_only
        .address_space:  global
        .offset:         16
        .size:           8
        .value_kind:     global_buffer
      - .offset:         24
        .size:           4
        .value_kind:     by_value
      - .offset:         28
        .size:           4
        .value_kind:     by_value
      - .actual_access:  read_only
        .address_space:  global
        .offset:         32
        .size:           8
        .value_kind:     global_buffer
      - .actual_access:  read_only
        .address_space:  global
        .offset:         40
        .size:           8
        .value_kind:     global_buffer
      - .actual_access:  read_only
        .address_space:  global
        .offset:         48
        .size:           8
        .value_kind:     global_buffer
      - .actual_access:  read_only
        .address_space:  global
        .offset:         56
        .size:           8
        .value_kind:     global_buffer
      - .actual_access:  write_only
        .address_space:  global
        .offset:         64
        .size:           8
        .value_kind:     global_buffer
      - .offset:         72
        .size:           4
        .value_kind:     by_value
      - .actual_access:  read_only
        .address_space:  global
        .offset:         80
        .size:           8
        .value_kind:     global_buffer
      - .offset:         88
        .size:           4
        .value_kind:     hidden_block_count_x
      - .offset:         92
        .size:           4
        .value_kind:     hidden_block_count_y
      - .offset:         96
        .size:           4
        .value_kind:     hidden_block_count_z
      - .offset:         100
        .size:           2
        .value_kind:     hidden_group_size_x
      - .offset:         102
        .size:           2
        .value_kind:     hidden_group_size_y
      - .offset:         104
        .size:           2
        .value_kind:     hidden_group_size_z
      - .offset:         106
        .size:           2
        .value_kind:     hidden_remainder_x
      - .offset:         108
        .size:           2
        .value_kind:     hidden_remainder_y
      - .offset:         110
        .size:           2
        .value_kind:     hidden_remainder_z
      - .offset:         128
        .size:           8
        .value_kind:     hidden_global_offset_x
      - .offset:         136
        .size:           8
        .value_kind:     hidden_global_offset_y
      - .offset:         144
        .size:           8
        .value_kind:     hidden_global_offset_z
      - .offset:         152
        .size:           2
        .value_kind:     hidden_grid_dims
    .group_segment_fixed_size: 16384
    .kernarg_segment_align: 8
    .kernarg_segment_size: 344
    .language:       OpenCL C
    .language_version:
      - 2
      - 0
    .max_flat_workgroup_size: 1024
    .name:           _Z13refine_kernelILi1ELi16ELi128ELb1ELi4EEvPKfiiS1_iiS1_PKiS3_S3_PfiPy
    .private_segment_fixed_size: 0
    .sgpr_count:     35
    .sgpr_spill_count: 0
    .symbol:         _Z13refine_kernelILi1ELi16ELi128ELb1ELi4EEvPKfiiS1_iiS1_PKiS3_S3_PfiPy.kd
    .uniform_work_group_size: 1
    .uses_dynamic_stack: false
    .vgpr_count:     64
    .vgpr_spill_count: 0
    .wavefront_size: 64
  - .agpr_count:     0
    .args:
      - .actual_access:  read_only
        .address_space:  global
        .offset:         0
        .size:           8
        .value_kind:     global_buffer
      - .offset:         8
        .size:           4
        .value_kind:     by_value
      - .offset:         12
        .size:           4
        .value_kind:     by_value
      - .actual_access:  read_only
        .address_space:  global
        .offset:         16
        .size:           8
        .value_kind:     global_buffer
      - .offset:         24
        .size:           4
        .value_kind:     by_value
      - .offset:         28
        .size:           4
        .value_kind:     by_value
      - .actual_access:  read_only
        .address_space:  global
        .offset:         32
        .size:           8
        .value_kind:     global_buffer
      - .actual_access:  read_only
        .address_space:  global
        .offset:         40
        .size:           8
        .value_kind:     global_buffer
      - .actual_access:  read_only
        .address_space:  global
        .offset:         48
        .size:           8
        .value_kind:     global_buffer
      - .actual_access:  read_only
        .address_space:  global
        .offset:         56
        .size:           8
        .value_kind:     global_buffer
      - .actual_access:  write_only
        .address_space:  global
        .offset:         64
        .size:           8
        .value_kind:     global_buffer
      - .offset:         72
        .size:           4
        .value_kind:     by_value
      - .actual_access:  read_only
        .address_space:  global
        .offset:         80
        .size:           8
        .value_kind:     global_buffer
      - .offset:         88
        .size:           4
        .value_kind:     hidden_block_count_x
      - .offset:         92
        .size:           4
        .value_kind:     hidden_block_count_y
      - .offset:         96
        .size:           4
        .value_kind:     hidden_block_count_z
      - .offset:         100
        .size:           2
        .value_kind:     hidden_group_size_x
      - .offset:         102
        .size:           2
        .value_kind:     hidden_group_size_y
      - .offset:         104
        .size:           2
        .value_kind:     hidden_group_size_z
      - .offset:         106
        .size:           2
        .value_kind:     hidden_remainder_x
      - .offset:         108
        .size:           2
        .value_kind:     hidden_remainder_y
      - .offset:         110
        .size:           2
        .value_kind:     hidden_remainder_z
      - .offset:         128
        .size:           8
        .value_kind:     hidden_global_offset_x
      - .offset:         136
        .size:           8
        .value_kind:     hidden_global_offset_y
      - .offset:         144
        .size:           8
        .value_kind:     hidden_global_offset_z
      - .offset:         152
        .size:           2
        .value_kind:     hidden_grid_dims
    .group_segment_fixed_size: 16384
    .kernarg_segment_align: 8
    .kernarg_segment_size: 344
    .language:       OpenCL C
    .language_version:
      - 2
      - 0
    .max_flat_workgroup_size: 1024
    .name:           _Z13refine_kernelILi2ELi16ELi64ELb0ELi4EEvPKfiiS1_iiS1_PKiS3_S3_PfiPy
    .private_segment_fixed_size: 0
    .sgpr_count:     35
    .sgpr_spill_count: 0
    .symbol:         _Z13refine_kernelILi2ELi16ELi64ELb0ELi4EEvPKfiiS1_iiS1_PKiS3_S3_PfiPy.kd
    .uniform_work_group_size: 1
    .uses_dynamic_stack: false
    .vgpr_count:     85
    .vgpr_spill_count: 0
    .wavefront_size: 64
  - .agpr_count:     0
    .args:
      - .actual_access:  read_only
        .address_space:  global
        .offset:         0
        .size:           8
        .value_kind:     global_buffer
      - .offset:         8
        .size:           4
        .value_kind:     by_value
      - .offset:         12
        .size:           4
        .value_kind:     by_value
      - .actual_access:  read_only
        .address_space:  global
        .offset:         16
        .size:           8
        .value_kind:     global_buffer
      - .offset:         24
        .size:           4
        .value_kind:     by_value
      - .offset:         28
        .size:           4
        .value_kind:     by_value
      - .actual_access:  read_only
        .address_space:  global
        .offset:         32
        .size:           8
        .value_kind:     global_buffer
      - .actual_access:  read_only
        .address_space:  global
        .offset:         40
        .size:           8
        .value_kind:     global_buffer
      - .actual_access:  read_only
        .address_space:  global
        .offset:         48
        .size:           8
        .value_kind:     global_buffer
      - .actual_access:  read_only
        .address_space:  global
        .offset:         56
        .size:           8
        .value_kind:     global_buffer
      - .actual_access:  read_only
        .address_space:  global
        .offset:         64
        .size:           8
        .value_kind:     global_buffer
      - .offset:         72
        .size:           4
        .value_kind:     by_value
      - .address_space:  global
        .offset:         80
        .size:           8
        .value_kind:     global_buffer
      - .offset:         88
        .size:           4
        .value_kind:     hidden_block_count_x
      - .offset:         92
        .size:           4
        .value_kind:     hidden_block_count_y
      - .offset:         96
        .size:           4
        .value_kind:     hidden_block_count_z
      - .offset:         100
        .size:           2
        .value_kind:     hidden_group_size_x
      - .offset:         102
        .size:           2
        .value_kind:     hidden_group_size_y
      - .offset:         104
        .size:           2
        .value_kind:     hidden_group_size_z
      - .offset:         106
        .size:           2
        .value_kind:     hidden_remainder_x
      - .offset:         108
        .size:           2
        .value_kind:     hidden_remainder_y
      - .offset:         110
        .size:           2
        .value_kind:     hidden_remainder_z
      - .offset:         128
        .size:           8
        .value_kind:     hidden_global_offset_x
      - .offset:         136
        .size:           8
        .value_kind:     hidden_global_offset_y
      - .offset:         144
        .size:           8
        .value_kind:     hidden_global_offset_z
      - .offset:         152
        .size:           2
        .value_kind:     hidden_grid_dims
    .group_segment_fixed_size: 8192
    .kernarg_segment_align: 8
    .kernarg_segment_size: 344
    .language:       OpenCL C
    .language_version:
      - 2
      - 0
    .max_flat_workgroup_size: 512
    .name:           _Z13refine_kernelILi3ELi8ELi64ELb0ELi4EEvPKfiiS1_iiS1_PKiS3_S3_PfiPy
    .private_segment_fixed_size: 0
    .sgpr_count:     38
    .sgpr_spill_count: 0
    .symbol:         _Z13refine_kernelILi3ELi8ELi64ELb0ELi4EEvPKfiiS1_iiS1_PKiS3_S3_PfiPy.kd
    .uniform_work_group_size: 1
    .uses_dynamic_stack: false
    .vgpr_count:     88
    .vgpr_spill_count: 0
    .wavefront_size: 64
